# poll back-off doubled (s_sleep 12 / 6) and the MoE down-tile flag wait polls every s_sleep 4 instead of 1
# baseline (speedup 1.0000x reference)
;     template <class T> __device__ __forceinline__ T* w(size_t off) const { return (T*)(p->ws + off); }
; __device__ __forceinline__ void ph_moe2_mfma(const Ctx& c, int layer, int tile, const int* sm, unsigned char* lds) {
;     ...
;         unsigned* flag = c.w<unsigned>(WS_CTL) + CW_MOEF + (layer * 512 + st) * 16;
;         if (c.tid == 0) {
;             unsigned sp = 0u;
;             while (__hip_atomic_load(flag, __ATOMIC_RELAXED, __HIP_MEMORY_SCOPE_AGENT) < 8u) { __builtin_amdgcn_s_sleep(1); if (++sp > (1u << 22)) break; }
;             __builtin_amdgcn_fence(__ATOMIC_ACQUIRE, "agent");
;         }
.LBB0_145:
	global_load_dword v2, v3, s[44:45] sc1
	s_mov_b64 s[46:47], -1
	s_waitcnt vmcnt(0)
	v_cmp_lt_u32_e32 vcc, 7, v2
	s_cbranch_vccnz .LBB0_144
	s_sleep 4
	global_load_dword v2, v3, s[44:45] sc1
	s_waitcnt vmcnt(0)
	v_cmp_gt_u32_e32 vcc, 8, v2
	s_cbranch_vccz .LBB0_144
	s_sleep 4
	global_load_dword v2, v3, s[44:45] sc1
	s_waitcnt vmcnt(0)
	v_cmp_gt_u32_e32 vcc, 8, v2
	s_cbranch_vccz .LBB0_144
	s_sleep 4
	global_load_dword v2, v3, s[44:45] sc1
	s_waitcnt vmcnt(0)
	v_cmp_gt_u32_e32 vcc, 8, v2
	s_cbranch_vccz .LBB0_144
	s_sleep 4
	global_load_dword v2, v3, s[44:45] sc1
	s_waitcnt vmcnt(0)
	v_cmp_gt_u32_e32 vcc, 8, v2
	s_cbranch_vccz .LBB0_144
	s_add_i32 s6, s6, -5
	s_cmp_eq_u32 s6, 0
	s_cselect_b64 s[46:47], -1, 0
	s_sleep 4
	s_branch .LBB0_144

; __device__ __forceinline__ unsigned xb_ld(unsigned* p)              { return __hip_atomic_load(p, __ATOMIC_RELAXED, __HIP_MEMORY_SCOPE_AGENT); }
; __device__ __forceinline__ unsigned xb_add(unsigned* p, unsigned v) { return __hip_atomic_fetch_add(p, v, __ATOMIC_RELAXED, __HIP_MEMORY_SCOPE_AGENT); }
; #define XB_SPIN(cond, bar) do { unsigned _sp = 0; while (cond) { __builtin_amdgcn_s_sleep(1); \
;     if ((++_sp & 255u) == 0u) { if (xb_ld(&(bar)[XB_TMO])) break; if (_sp > XB_SPIN_CAP) { atomicAdd(&(bar)[XB_TMO], 1u); break; } } } } while (0)
; __device__ __forceinline__ void xcd_barrier(const XcdBarrier& b) {
;     asm volatile("s_waitcnt vmcnt(0)" ::: "memory");
;     __syncthreads();
;     if (threadIdx.x == 0) {
;         unsigned* bar = b.bar;
;         __builtin_amdgcn_s_waitcnt(0);
;         unsigned nloc = b.st[0], nx = b.st[1];
;         if (nloc == 0u) { xcd_barrier_complete(bar, b.x, nloc, nx); b.st[0] = nloc; b.st[1] = nx; }
;         const unsigned old = xb_add(&bar[XB_XSUB(b.x)], 1u);
;         const unsigned gen = old / nloc;
;         if (old + 1u == (gen + 1u) * nloc) {
;             __builtin_amdgcn_fence(__ATOMIC_RELEASE, "agent");
;             asm volatile("s_waitcnt vmcnt(0)" ::: "memory");
;             const unsigned og = xb_add(&bar[XB_TOP], 1u);
;             const unsigned tg = og / nx;
;             if (og + 1u == (tg + 1u) * nx) xb_add(&bar[XB_TOPGEN], 1u);
;             else XB_SPIN(xb_ld(&bar[XB_TOPGEN]) == tg, bar);
;             __builtin_amdgcn_fence(__ATOMIC_ACQUIRE, "agent");
;             xb_add(&bar[XB_XGEN(b.x)], 1u);
;             asm volatile("s_waitcnt vmcnt(0)" ::: "memory");
;         } else {
;             XB_SPIN(xb_ld(&bar[XB_XGEN(b.x)]) == gen, bar);
;             __builtin_amdgcn_fence(__ATOMIC_ACQUIRE, "agent");
;             asm volatile("s_waitcnt vmcnt(0)" ::: "memory");
;         }
.Lxb_poll:
	global_load_dword v6, v3, s[42:43] sc1
	s_waitcnt vmcnt(0)
	v_cmp_ge_u32_e32 vcc, v6, v5
	s_cbranch_vccnz .Lxb_done
	s_add_i32 s15, s15, 1
	s_cmp_lt_u32 s15, 0x400000
	s_cbranch_scc0 .Lxb_done
	s_sleep 12
	s_branch .Lxb_poll

; __device__ __forceinline__ unsigned xb_ld(unsigned* p)              { return __hip_atomic_load(p, __ATOMIC_RELAXED, __HIP_MEMORY_SCOPE_AGENT); }
; __device__ __forceinline__ unsigned xb_add(unsigned* p, unsigned v) { return __hip_atomic_fetch_add(p, v, __ATOMIC_RELAXED, __HIP_MEMORY_SCOPE_AGENT); }
; #define XB_SPIN(cond, bar) do { unsigned _sp = 0; while (cond) { __builtin_amdgcn_s_sleep(1); \
;     if ((++_sp & 255u) == 0u) { if (xb_ld(&(bar)[XB_TMO])) break; if (_sp > XB_SPIN_CAP) { atomicAdd(&(bar)[XB_TMO], 1u); break; } } } } while (0)
; __device__ __forceinline__ void xcd_barrier(const XcdBarrier& b) {
;     asm volatile("s_waitcnt vmcnt(0)" ::: "memory");
;     __syncthreads();
;     if (threadIdx.x == 0) {
;         unsigned* bar = b.bar;
;         __builtin_amdgcn_s_waitcnt(0);
;         unsigned nloc = b.st[0], nx = b.st[1];
;         if (nloc == 0u) { xcd_barrier_complete(bar, b.x, nloc, nx); b.st[0] = nloc; b.st[1] = nx; }
;         const unsigned old = xb_add(&bar[XB_XSUB(b.x)], 1u);
;         const unsigned gen = old / nloc;
;         if (old + 1u == (gen + 1u) * nloc) {
;             __builtin_amdgcn_fence(__ATOMIC_RELEASE, "agent");
;             asm volatile("s_waitcnt vmcnt(0)" ::: "memory");
;             const unsigned og = xb_add(&bar[XB_TOP], 1u);
;             const unsigned tg = og / nx;
;             if (og + 1u == (tg + 1u) * nx) xb_add(&bar[XB_TOPGEN], 1u);
;             else XB_SPIN(xb_ld(&bar[XB_TOPGEN]) == tg, bar);
;             __builtin_amdgcn_fence(__ATOMIC_ACQUIRE, "agent");
;             xb_add(&bar[XB_XGEN(b.x)], 1u);
;             asm volatile("s_waitcnt vmcnt(0)" ::: "memory");
;         } else {
;             XB_SPIN(xb_ld(&bar[XB_XGEN(b.x)]) == gen, bar);
;             __builtin_amdgcn_fence(__ATOMIC_ACQUIRE, "agent");
;             asm volatile("s_waitcnt vmcnt(0)" ::: "memory");
;         }
.Lxb_poll_cu:
	global_load_dword v6, v3, s[44:45] sc1
	s_waitcnt vmcnt(0)
	v_cmp_ge_u32_e32 vcc, v6, v255
	s_cbranch_vccnz .Lxb_out
	s_add_i32 s15, s15, 1
	s_cmp_lt_u32 s15, 0x400000
	s_cbranch_scc0 .Lxb_out
	s_sleep 6
	s_branch .Lxb_poll_cu
